# P10 SwiGLU epilogue: (y+1)*4 computed with one v_fma_f32 instead of add then mul (58 sites, bit-identical)
# baseline (speedup 1.0000x reference)
; __device__ __forceinline__ unsigned pk4f8(float a, float b, float c, float d) { int r = 0; r = __builtin_amdgcn_cvt_pk_fp8_f32(a, b, r, false); r = __builtin_amdgcn_cvt_pk_fp8_f32(c, d, r, true); return (unsigned)r; }
; __device__ __forceinline__ float sigm(float x) { return __builtin_amdgcn_rcpf(1.f + __expf(-x)); }
;     __device__ __forceinline__ void operator()(const f32x4 (&acc)[2][2][4][2], const Unit& u, int wr, int wc, int fr, int fq) const {
;         const int row0 = u.pm * BM + wr * 64 + fr, colg = u.pn * 128 + wc * 32 + 8 * fq; const int e = tile_e[u.pm];
;         const float* bp = bgu + (size_t)e * 4096 + colg;
;         const f32x4 bg0 = *(const f32x4*)(bp), bg1 = *(const f32x4*)(bp + 4), bu0 = *(const f32x4*)(bp + 2048), bu1 = *(const f32x4*)(bp + 2052);
; #pragma unroll
;         for (int ai = 0; ai < 2; ++ai)
; #pragma unroll
;             for (int m = 0; m < 4; ++m) { const size_t r = (size_t)(row0 + ai * HALF + m * 16);
;                 constexpr float DS = 1.f / (F8_SX * F8_SW);
;                 const f32x4 ga = acc[ai][0][m][0] * DS + bg0, gb = acc[ai][0][m][1] * DS + bg1, ua = acc[ai][1][m][0] * DS + bu0, ub = acc[ai][1][m][1] * DS + bu1;
;                 float o[8];
; #pragma unroll
;                 for (int j = 0; j < 4; ++j) { const float g = fminf(ga[j], 7.f), up = fminf(fmaxf(ua[j], -7.f), 7.f); o[j] = F8_SA * (up + 1.f) * g * sigm(1.702f * g);
;                                               const float g2 = fminf(gb[j], 7.f), up2 = fminf(fmaxf(ub[j], -7.f), 7.f); o[4 + j] = F8_SA * (up2 + 1.f) * g2 * sigm(1.702f * g2); }
;                 v2u w; w.x = pk4f8(o[0], o[1], o[2], o[3]); w.y = pk4f8(o[4], o[5], o[6], o[7]);
;                 *(v2u*)(ACT + r * FF + colg) = w; }
.LBB0_1922:
	s_lshl_b32 s2, s43, 2
	s_add_i32 s2, s2, 0
	s_add_i32 s2, s2, 0x20100
	s_nop 15
	s_nop 15
	v_mov_b32_e32 v2, s2
	ds_read_b32 v2, v2
	v_lshl_or_b32 v20, s0, 7, v196
	v_ashrrev_i32_e32 v21, 31, v20
	v_lshl_add_u32 v22, s43, 8, v194
	s_waitcnt lgkmcnt(0)
	v_ashrrev_i32_e32 v3, 31, v2
	v_lshlrev_b64 v[2:3], 14, v[2:3]
	v_lshl_add_u64 v[2:3], s[80:81], 0, v[2:3]
	v_lshl_add_u64 v[2:3], v[20:21], 2, v[2:3]
	global_load_dwordx4 v[14:17], v[2:3], off
	global_load_dwordx4 v[6:9], v[2:3], off offset:16
	v_add_co_u32_e32 v4, vcc, s52, v2
	s_nop 1
	v_addc_co_u32_e32 v5, vcc, 0, v3, vcc
	v_lshl_add_u64 v[2:3], v[2:3], 0, s[38:39]
	global_load_dwordx4 v[10:13], v[4:5], off
	global_load_dwordx4 v[2:5], v[2:3], off offset:16
	s_waitcnt vmcnt(2)
	v_fmamk_f32 v18, v158, 0x3a000000, v14
	v_fmamk_f32 v24, v155, 0x3a000000, v7
	v_min_f32_e32 v18, 0x40e00000, v18
	v_min_f32_e32 v24, 0x40e00000, v24
	v_fmamk_f32 v19, v154, 0x3a000000, v6
	v_fmamk_f32 v25, v160, 0x3a000000, v16
	v_mul_f32_e32 v175, 0x3fd9db23, v18
	v_mul_f32_e32 v183, 0x3fd9db23, v24
	v_min_f32_e32 v19, 0x40e00000, v19
	v_min_f32_e32 v25, 0x40e00000, v25
	v_mul_f32_e32 v175, 0xbfb8aa3b, v175
	v_mul_f32_e32 v183, 0xbfb8aa3b, v183
	v_mul_f32_e32 v177, 0x3fd9db23, v19
	v_mul_f32_e32 v184, 0x3fd9db23, v25
	v_exp_f32_e32 v175, v175
	v_exp_f32_e32 v183, v183
	v_fmamk_f32 v27, v161, 0x3a000000, v17
	v_mul_f32_e32 v177, 0xbfb8aa3b, v177
	v_mul_f32_e32 v184, 0xbfb8aa3b, v184
	v_min_f32_e32 v27, 0x40e00000, v27
	v_exp_f32_e32 v177, v177
	v_exp_f32_e32 v184, v184
	v_fmamk_f32 v23, v159, 0x3a000000, v15
	v_mul_f32_e32 v186, 0x3fd9db23, v27
	v_min_f32_e32 v23, 0x40e00000, v23
	v_mul_f32_e32 v186, 0xbfb8aa3b, v186
	v_mul_f32_e32 v182, 0x3fd9db23, v23
	v_exp_f32_e32 v186, v186
	v_mul_f32_e32 v182, 0xbfb8aa3b, v182
	v_exp_f32_e32 v182, v182
	v_fmamk_f32 v26, v156, 0x3a000000, v8
	v_min_f32_e32 v26, 0x40e00000, v26
	v_mul_f32_e32 v185, 0x3fd9db23, v26
	v_mul_f32_e32 v185, 0xbfb8aa3b, v185
	v_exp_f32_e32 v185, v185
	s_waitcnt vmcnt(1)
	v_fmamk_f32 v28, v126, 0x3a000000, v10
	v_med3_f32 v28, v28, s55, v199
	s_waitcnt vmcnt(0)
	v_fmamk_f32 v31, v123, 0x3a000000, v3
	v_med3_f32 v31, v31, s55, v199
	v_fmamk_f32 v29, v122, 0x3a000000, v2
	v_fmamk_f32 v32, v128, 0x3a000000, v12
	v_med3_f32 v29, v29, s55, v199
	v_med3_f32 v32, v32, s55, v199
	v_fma_f32 v28, v28, 4.0, 4.0
	v_fma_f32 v31, v31, 4.0, 4.0
	v_mul_f32_e32 v18, v18, v28
	v_mul_f32_e32 v24, v24, v31
	v_add_f32_e32 v28, 1.0, v175
	v_add_f32_e32 v31, 1.0, v183
	v_fma_f32 v29, v29, 4.0, 4.0
	v_fma_f32 v32, v32, 4.0, 4.0
	v_rcp_f32_e32 v28, v28
	v_rcp_f32_e32 v31, v31
	v_mul_f32_e32 v19, v19, v29
	v_mul_f32_e32 v25, v25, v32
	v_add_f32_e32 v29, 1.0, v177
	v_add_f32_e32 v32, 1.0, v184
	v_fmamk_f32 v30, v127, 0x3a000000, v11
	v_rcp_f32_e32 v29, v29
	v_rcp_f32_e32 v32, v32
	v_med3_f32 v30, v30, s55, v199
	v_fmamk_f32 v173, v129, 0x3a000000, v13
	v_mul_f32_e32 v18, v28, v18
	v_mul_f32_e32 v28, v31, v24
	v_add_f32_e32 v24, 1.0, v186
	v_med3_f32 v173, v173, s55, v199
	v_fma_f32 v30, v30, 4.0, 4.0
	v_rcp_f32_e32 v24, v24
	v_mul_f32_e32 v23, v23, v30
	v_add_f32_e32 v30, 1.0, v182
	v_mul_f32_e32 v19, v29, v19
	v_mul_f32_e32 v29, v32, v25
	v_add_f32_e32 v25, 1.0, v173
	v_rcp_f32_e32 v30, v30
	v_mul_f32_e32 v25, 4.0, v25
	v_mul_f32_e32 v25, v27, v25
	v_mul_f32_e32 v27, v24, v25
	v_fmamk_f32 v24, v157, 0x3a000000, v9
	v_min_f32_e32 v24, 0x40e00000, v24
	v_mul_f32_e32 v23, v30, v23
	v_mul_f32_e32 v30, 0x3fd9db23, v24
	v_mul_f32_e32 v30, 0xbfb8aa3b, v30
	v_fmamk_f32 v33, v124, 0x3a000000, v4
	v_fmamk_f32 v25, v125, 0x3a000000, v5
	v_exp_f32_e32 v30, v30
	v_med3_f32 v33, v33, s55, v199
	v_med3_f32 v25, v25, s55, v199
	v_fma_f32 v33, v33, 4.0, 4.0
	v_fma_f32 v25, v25, 4.0, 4.0
	v_mul_f32_e32 v26, v26, v33
	v_add_f32_e32 v33, 1.0, v185
	v_mul_f32_e32 v31, v24, v25
	v_add_f32_e32 v24, 1.0, v30
	v_rcp_f32_e32 v33, v33
	v_rcp_f32_e32 v30, v24
	v_mov_b32_e32 v24, v171
	v_mov_b32_e32 v25, v171
	v_cvt_pk_fp8_f32 v24, v18, v23
	v_cvt_pk_fp8_f32 v25, v19, v28
	v_mul_f32_e32 v26, v33, v26
	v_mul_f32_e32 v18, v30, v31
	v_ashrrev_i32_e32 v23, 31, v22
	v_cvt_pk_fp8_f32 v24, v29, v27 op_sel:[0,0,1]
	v_cvt_pk_fp8_f32 v25, v26, v18 op_sel:[0,0,1]
	v_lshlrev_b64 v[18:19], 11, v[22:23]
	v_lshl_add_u64 v[18:19], s[22:23], 0, v[18:19]
	v_fmamk_f32 v23, v150, 0x3a000000, v14
	v_lshl_add_u64 v[18:19], v[18:19], 0, v[20:21]
	v_min_f32_e32 v23, 0x40e00000, v23
	global_store_dwordx2 v[18:19], v[24:25], off
	v_mul_f32_e32 v24, 0x3fd9db23, v23
	v_mul_f32_e32 v24, 0xbfb8aa3b, v24
	v_exp_f32_e32 v25, v24
	v_fmamk_f32 v26, v118, 0x3a000000, v10
	v_med3_f32 v26, v26, s55, v199
	v_add_f32_e32 v25, 1.0, v25
	v_rcp_f32_e32 v25, v25
	v_fma_f32 v26, v26, 4.0, 4.0
	v_mul_f32_e32 v23, v23, v26
	v_fmamk_f32 v26, v114, 0x3a000000, v2
	v_mul_f32_e32 v23, v25, v23
	v_fmamk_f32 v25, v146, 0x3a000000, v6
	v_min_f32_e32 v25, 0x40e00000, v25
	v_mul_f32_e32 v27, 0x3fd9db23, v25
	v_mul_f32_e32 v27, 0xbfb8aa3b, v27
	v_exp_f32_e32 v27, v27
	v_med3_f32 v26, v26, s55, v199
	v_fma_f32 v26, v26, 4.0, 4.0
	v_mul_f32_e32 v25, v25, v26
	v_add_f32_e32 v26, 1.0, v27
	v_fmamk_f32 v27, v151, 0x3a000000, v15
	v_min_f32_e32 v27, 0x40e00000, v27
	v_mul_f32_e32 v28, 0x3fd9db23, v27
	v_mul_f32_e32 v28, 0xbfb8aa3b, v28
	v_rcp_f32_e32 v26, v26
	v_exp_f32_e32 v28, v28
	v_or_b32_e32 v24, 16, v22
	v_mul_f32_e32 v25, v26, v25
	v_fmamk_f32 v26, v119, 0x3a000000, v11
	v_add_f32_e32 v28, 1.0, v28
	v_med3_f32 v26, v26, s55, v199
	v_rcp_f32_e32 v28, v28
	v_fma_f32 v26, v26, 4.0, 4.0
	v_mul_f32_e32 v26, v27, v26
	v_mul_f32_e32 v27, v28, v26
	v_fmamk_f32 v26, v147, 0x3a000000, v7
	v_min_f32_e32 v26, 0x40e00000, v26
	v_mul_f32_e32 v29, 0x3fd9db23, v26
; __device__ __forceinline__ unsigned pk4f8(float a, float b, float c, float d) { int r = 0; r = __builtin_amdgcn_cvt_pk_fp8_f32(a, b, r, false); r = __builtin_amdgcn_cvt_pk_fp8_f32(c, d, r, true); return (unsigned)r; }
; __device__ __forceinline__ float sigm(float x) { return __builtin_amdgcn_rcpf(1.f + __expf(-x)); }
;     __device__ __forceinline__ void operator()(const f32x4 (&acc)[2][2][4][2], const Unit& u, int wr, int wc, int fr, int fq) const {
;     ...
;             for (int m = 0; m < 4; ++m) { const size_t r = (size_t)(row0 + ai * HALF + m * 16);
;                 constexpr float DS = 1.f / (F8_SX * F8_SW);
;                 const f32x4 ga = acc[ai][0][m][0] * DS + bg0, gb = acc[ai][0][m][1] * DS + bg1, ua = acc[ai][1][m][0] * DS + bu0, ub = acc[ai][1][m][1] * DS + bu1;
;                 float o[8];
; #pragma unroll
;                 for (int j = 0; j < 4; ++j) { const float g = fminf(ga[j], 7.f), up = fminf(fmaxf(ua[j], -7.f), 7.f); o[j] = F8_SA * (up + 1.f) * g * sigm(1.702f * g);
;                                               const float g2 = fminf(gb[j], 7.f), up2 = fminf(fmaxf(ub[j], -7.f), 7.f); o[4 + j] = F8_SA * (up2 + 1.f) * g2 * sigm(1.702f * g2); }
;                 v2u w; w.x = pk4f8(o[0], o[1], o[2], o[3]); w.y = pk4f8(o[4], o[5], o[6], o[7]);
;                 *(v2u*)(ACT + r * FF + colg) = w; }
	v_mul_f32_e32 v29, 0xbfb8aa3b, v29
	v_fmamk_f32 v28, v115, 0x3a000000, v3
	v_exp_f32_e32 v29, v29
	v_med3_f32 v28, v28, s55, v199
	v_fma_f32 v28, v28, 4.0, 4.0
	v_mul_f32_e32 v26, v26, v28
	v_add_f32_e32 v28, 1.0, v29
	v_fmamk_f32 v29, v152, 0x3a000000, v16
	v_min_f32_e32 v29, 0x40e00000, v29
	v_mul_f32_e32 v30, 0x3fd9db23, v29
	v_mul_f32_e32 v30, 0xbfb8aa3b, v30
	v_rcp_f32_e32 v28, v28
	v_exp_f32_e32 v30, v30
	v_mul_f32_e32 v28, v28, v26
	v_fmamk_f32 v26, v120, 0x3a000000, v12
	v_add_f32_e32 v30, 1.0, v30
	v_med3_f32 v26, v26, s55, v199
	v_rcp_f32_e32 v30, v30
	v_fma_f32 v26, v26, 4.0, 4.0
	v_mul_f32_e32 v26, v29, v26
	v_mul_f32_e32 v29, v30, v26
	v_fmamk_f32 v26, v148, 0x3a000000, v8
	v_min_f32_e32 v26, 0x40e00000, v26
	v_mul_f32_e32 v31, 0x3fd9db23, v26
	v_mul_f32_e32 v31, 0xbfb8aa3b, v31
	v_fmamk_f32 v30, v116, 0x3a000000, v4
	v_exp_f32_e32 v31, v31
	v_med3_f32 v30, v30, s55, v199
	v_fma_f32 v30, v30, 4.0, 4.0
	v_mul_f32_e32 v26, v26, v30
	v_add_f32_e32 v30, 1.0, v31
	v_fmamk_f32 v31, v153, 0x3a000000, v17
	v_min_f32_e32 v31, 0x40e00000, v31
	v_mul_f32_e32 v32, 0x3fd9db23, v31
	v_mul_f32_e32 v32, 0xbfb8aa3b, v32
	v_rcp_f32_e32 v30, v30
	v_exp_f32_e32 v32, v32
	v_mul_f32_e32 v30, v30, v26
	v_fmamk_f32 v26, v121, 0x3a000000, v13
	v_add_f32_e32 v32, 1.0, v32
	v_med3_f32 v26, v26, s55, v199
	v_rcp_f32_e32 v32, v32
	v_fma_f32 v26, v26, 4.0, 4.0
	v_mul_f32_e32 v26, v31, v26
	v_mul_f32_e32 v31, v32, v26
	v_fmamk_f32 v26, v149, 0x3a000000, v9
	v_min_f32_e32 v26, 0x40e00000, v26
	v_mul_f32_e32 v33, 0x3fd9db23, v26
	v_mul_f32_e32 v33, 0xbfb8aa3b, v33
	v_fmamk_f32 v32, v117, 0x3a000000, v5
	v_exp_f32_e32 v33, v33
	v_med3_f32 v32, v32, s55, v199
	v_fma_f32 v32, v32, 4.0, 4.0
	v_mul_f32_e32 v32, v26, v32
	v_add_f32_e32 v26, 1.0, v33
	v_rcp_f32_e32 v33, v26
	v_mov_b32_e32 v26, v171
	v_cvt_pk_fp8_f32 v26, v23, v27
	v_mov_b32_e32 v27, v171
	v_cvt_pk_fp8_f32 v27, v25, v28
	v_mul_f32_e32 v23, v33, v32
	v_ashrrev_i32_e32 v25, 31, v24
	v_cvt_pk_fp8_f32 v26, v29, v31 op_sel:[0,0,1]
	v_cvt_pk_fp8_f32 v27, v30, v23 op_sel:[0,0,1]
	v_lshlrev_b64 v[24:25], 11, v[24:25]
	v_lshl_add_u64 v[24:25], s[22:23], 0, v[24:25]
	v_fmamk_f32 v23, v142, 0x3a000000, v14
	v_lshl_add_u64 v[24:25], v[24:25], 0, v[20:21]
	v_min_f32_e32 v23, 0x40e00000, v23
	global_store_dwordx2 v[24:25], v[26:27], off
	v_mul_f32_e32 v24, 0x3fd9db23, v23
	v_mul_f32_e32 v24, 0xbfb8aa3b, v24
	v_exp_f32_e32 v25, v24
	v_fmamk_f32 v26, v110, 0x3a000000, v10
	v_med3_f32 v26, v26, s55, v199
	v_add_f32_e32 v25, 1.0, v25
	v_rcp_f32_e32 v25, v25
	v_fma_f32 v26, v26, 4.0, 4.0
	v_mul_f32_e32 v23, v23, v26
	v_fmamk_f32 v26, v106, 0x3a000000, v2
	v_mul_f32_e32 v23, v25, v23
	v_fmamk_f32 v25, v138, 0x3a000000, v6
	v_min_f32_e32 v25, 0x40e00000, v25
	v_mul_f32_e32 v27, 0x3fd9db23, v25
	v_mul_f32_e32 v27, 0xbfb8aa3b, v27
	v_exp_f32_e32 v27, v27
	v_med3_f32 v26, v26, s55, v199
	v_fma_f32 v26, v26, 4.0, 4.0
	v_mul_f32_e32 v25, v25, v26
	v_add_f32_e32 v26, 1.0, v27
	v_fmamk_f32 v27, v143, 0x3a000000, v15
	v_min_f32_e32 v27, 0x40e00000, v27
	v_mul_f32_e32 v28, 0x3fd9db23, v27
	v_mul_f32_e32 v28, 0xbfb8aa3b, v28
	v_rcp_f32_e32 v26, v26
	v_exp_f32_e32 v28, v28
	v_or_b32_e32 v24, 32, v22
	v_or_b32_e32 v22, 48, v22
	v_mul_f32_e32 v25, v26, v25
	v_fmamk_f32 v26, v111, 0x3a000000, v11
	v_add_f32_e32 v28, 1.0, v28
	v_med3_f32 v26, v26, s55, v199
	v_rcp_f32_e32 v28, v28
	v_fma_f32 v26, v26, 4.0, 4.0
	v_mul_f32_e32 v26, v27, v26
	v_mul_f32_e32 v27, v28, v26
	v_fmamk_f32 v26, v139, 0x3a000000, v7
	v_min_f32_e32 v26, 0x40e00000, v26
	v_mul_f32_e32 v29, 0x3fd9db23, v26
	v_mul_f32_e32 v29, 0xbfb8aa3b, v29
	v_fmamk_f32 v28, v107, 0x3a000000, v3
	v_exp_f32_e32 v29, v29
	v_med3_f32 v28, v28, s55, v199
	v_fma_f32 v28, v28, 4.0, 4.0
	v_mul_f32_e32 v26, v26, v28
	v_add_f32_e32 v28, 1.0, v29
	v_fmamk_f32 v29, v144, 0x3a000000, v16
	v_min_f32_e32 v29, 0x40e00000, v29
	v_mul_f32_e32 v30, 0x3fd9db23, v29
	v_mul_f32_e32 v30, 0xbfb8aa3b, v30
	v_rcp_f32_e32 v28, v28
	v_exp_f32_e32 v30, v30
	v_mul_f32_e32 v28, v28, v26
	v_fmamk_f32 v26, v112, 0x3a000000, v12
	v_add_f32_e32 v30, 1.0, v30
	v_med3_f32 v26, v26, s55, v199
	v_rcp_f32_e32 v30, v30
	v_fma_f32 v26, v26, 4.0, 4.0
	v_mul_f32_e32 v26, v29, v26
	v_mul_f32_e32 v29, v30, v26
	v_fmamk_f32 v26, v140, 0x3a000000, v8
	v_min_f32_e32 v26, 0x40e00000, v26
	v_mul_f32_e32 v31, 0x3fd9db23, v26
	v_mul_f32_e32 v31, 0xbfb8aa3b, v31
	v_fmamk_f32 v30, v108, 0x3a000000, v4
	v_exp_f32_e32 v31, v31
	v_med3_f32 v30, v30, s55, v199
	v_fma_f32 v30, v30, 4.0, 4.0
	v_mul_f32_e32 v26, v26, v30
	v_add_f32_e32 v30, 1.0, v31
	v_fmamk_f32 v31, v145, 0x3a000000, v17
	v_min_f32_e32 v31, 0x40e00000, v31
	v_mul_f32_e32 v32, 0x3fd9db23, v31
	v_mul_f32_e32 v32, 0xbfb8aa3b, v32
	v_rcp_f32_e32 v30, v30
	v_exp_f32_e32 v32, v32
	v_mul_f32_e32 v30, v30, v26
	v_fmamk_f32 v26, v113, 0x3a000000, v13
	v_add_f32_e32 v32, 1.0, v32
	v_med3_f32 v26, v26, s55, v199
	v_rcp_f32_e32 v32, v32
	v_fma_f32 v26, v26, 4.0, 4.0
	v_mul_f32_e32 v26, v31, v26
	v_mul_f32_e32 v31, v32, v26
	v_fmamk_f32 v26, v141, 0x3a000000, v9
	v_min_f32_e32 v26, 0x40e00000, v26
	v_mul_f32_e32 v33, 0x3fd9db23, v26
	v_mul_f32_e32 v33, 0xbfb8aa3b, v33
	v_fmamk_f32 v32, v109, 0x3a000000, v5
	v_exp_f32_e32 v33, v33
	v_med3_f32 v32, v32, s55, v199
	v_fma_f32 v32, v32, 4.0, 4.0
	v_mul_f32_e32 v32, v26, v32
	v_add_f32_e32 v26, 1.0, v33
	v_rcp_f32_e32 v33, v26
	v_mov_b32_e32 v26, v171
	v_cvt_pk_fp8_f32 v26, v23, v27
	v_mov_b32_e32 v27, v171
	v_cvt_pk_fp8_f32 v27, v25, v28
	v_mul_f32_e32 v23, v33, v32
	v_ashrrev_i32_e32 v25, 31, v24
	v_cvt_pk_fp8_f32 v26, v29, v31 op_sel:[0,0,1]
	v_cvt_pk_fp8_f32 v27, v30, v23 op_sel:[0,0,1]
	v_lshlrev_b64 v[24:25], 11, v[24:25]
; __device__ __forceinline__ unsigned pk4f8(float a, float b, float c, float d) { int r = 0; r = __builtin_amdgcn_cvt_pk_fp8_f32(a, b, r, false); r = __builtin_amdgcn_cvt_pk_fp8_f32(c, d, r, true); return (unsigned)r; }
; __device__ __forceinline__ float sigm(float x) { return __builtin_amdgcn_rcpf(1.f + __expf(-x)); }
;     __device__ __forceinline__ void operator()(const f32x4 (&acc)[2][2][4][2], const Unit& u, int wr, int wc, int fr, int fq) const {
;     ...
;             for (int m = 0; m < 4; ++m) { const size_t r = (size_t)(row0 + ai * HALF + m * 16);
;                 constexpr float DS = 1.f / (F8_SX * F8_SW);
;                 const f32x4 ga = acc[ai][0][m][0] * DS + bg0, gb = acc[ai][0][m][1] * DS + bg1, ua = acc[ai][1][m][0] * DS + bu0, ub = acc[ai][1][m][1] * DS + bu1;
;                 float o[8];
; #pragma unroll
;                 for (int j = 0; j < 4; ++j) { const float g = fminf(ga[j], 7.f), up = fminf(fmaxf(ua[j], -7.f), 7.f); o[j] = F8_SA * (up + 1.f) * g * sigm(1.702f * g);
;                                               const float g2 = fminf(gb[j], 7.f), up2 = fminf(fmaxf(ub[j], -7.f), 7.f); o[4 + j] = F8_SA * (up2 + 1.f) * g2 * sigm(1.702f * g2); }
;                 v2u w; w.x = pk4f8(o[0], o[1], o[2], o[3]); w.y = pk4f8(o[4], o[5], o[6], o[7]);
;                 *(v2u*)(ACT + r * FF + colg) = w; }
	v_lshl_add_u64 v[24:25], s[22:23], 0, v[24:25]
	v_fmamk_f32 v23, v134, 0x3a000000, v14
	v_lshl_add_u64 v[24:25], v[24:25], 0, v[20:21]
	v_min_f32_e32 v23, 0x40e00000, v23
	global_store_dwordx2 v[24:25], v[26:27], off
	v_mul_f32_e32 v24, 0x3fd9db23, v23
	v_mul_f32_e32 v24, 0xbfb8aa3b, v24
	v_exp_f32_e32 v24, v24
	v_fmamk_f32 v25, v102, 0x3a000000, v10
	v_med3_f32 v25, v25, s55, v199
	v_add_f32_e32 v24, 1.0, v24
	v_rcp_f32_e32 v24, v24
	v_fma_f32 v25, v25, 4.0, 4.0
	v_mul_f32_e32 v23, v23, v25
	v_fmamk_f32 v25, v98, 0x3a000000, v2
	v_mul_f32_e32 v23, v24, v23
	v_fmamk_f32 v24, v130, 0x3a000000, v6
	v_min_f32_e32 v24, 0x40e00000, v24
	v_mul_f32_e32 v26, 0x3fd9db23, v24
	v_mul_f32_e32 v26, 0xbfb8aa3b, v26
	v_exp_f32_e32 v26, v26
	v_med3_f32 v25, v25, s55, v199
	v_fma_f32 v25, v25, 4.0, 4.0
	v_mul_f32_e32 v24, v24, v25
	v_add_f32_e32 v25, 1.0, v26
	v_fmamk_f32 v26, v135, 0x3a000000, v15
	v_min_f32_e32 v26, 0x40e00000, v26
	v_mul_f32_e32 v27, 0x3fd9db23, v26
	v_mul_f32_e32 v27, 0xbfb8aa3b, v27
	v_rcp_f32_e32 v25, v25
	v_exp_f32_e32 v27, v27
	v_mul_f32_e32 v28, v25, v24
	v_fmamk_f32 v24, v103, 0x3a000000, v11
	v_add_f32_e32 v25, 1.0, v27
	v_med3_f32 v24, v24, s55, v199
	v_rcp_f32_e32 v25, v25
	v_fma_f32 v24, v24, 4.0, 4.0
	v_mul_f32_e32 v24, v26, v24
	v_mul_f32_e32 v25, v25, v24
	v_fmamk_f32 v24, v131, 0x3a000000, v7
	v_min_f32_e32 v24, 0x40e00000, v24
	v_mul_f32_e32 v27, 0x3fd9db23, v24
	v_mul_f32_e32 v27, 0xbfb8aa3b, v27
	v_fmamk_f32 v26, v99, 0x3a000000, v3
	v_exp_f32_e32 v27, v27
	v_med3_f32 v26, v26, s55, v199
	v_fma_f32 v26, v26, 4.0, 4.0
	v_mul_f32_e32 v24, v24, v26
	v_add_f32_e32 v26, 1.0, v27
	v_fmamk_f32 v27, v136, 0x3a000000, v16
	v_min_f32_e32 v27, 0x40e00000, v27
	v_mul_f32_e32 v29, 0x3fd9db23, v27
	v_mul_f32_e32 v29, 0xbfb8aa3b, v29
	v_rcp_f32_e32 v26, v26
	v_exp_f32_e32 v29, v29
	v_mul_f32_e32 v26, v26, v24
	v_fmamk_f32 v24, v104, 0x3a000000, v12
	v_add_f32_e32 v29, 1.0, v29
	v_med3_f32 v24, v24, s55, v199
	v_rcp_f32_e32 v29, v29
	v_fma_f32 v24, v24, 4.0, 4.0
	v_mul_f32_e32 v24, v27, v24
	v_mul_f32_e32 v27, v29, v24
	v_fmamk_f32 v24, v132, 0x3a000000, v8
	v_min_f32_e32 v24, 0x40e00000, v24
	v_mul_f32_e32 v30, 0x3fd9db23, v24
	v_mul_f32_e32 v30, 0xbfb8aa3b, v30
	v_fmamk_f32 v29, v100, 0x3a000000, v4
	v_exp_f32_e32 v30, v30
	v_med3_f32 v29, v29, s55, v199
	v_fma_f32 v29, v29, 4.0, 4.0
	v_mul_f32_e32 v24, v24, v29
	v_add_f32_e32 v29, 1.0, v30
	v_fmamk_f32 v30, v137, 0x3a000000, v17
	v_min_f32_e32 v30, 0x40e00000, v30
	v_mul_f32_e32 v31, 0x3fd9db23, v30
	v_mul_f32_e32 v31, 0xbfb8aa3b, v31
	v_rcp_f32_e32 v29, v29
	v_exp_f32_e32 v31, v31
	v_mul_f32_e32 v29, v29, v24
	v_fmamk_f32 v24, v105, 0x3a000000, v13
	v_add_f32_e32 v31, 1.0, v31
	v_med3_f32 v24, v24, s55, v199
	v_rcp_f32_e32 v31, v31
	v_fma_f32 v24, v24, 4.0, 4.0
	v_mul_f32_e32 v24, v30, v24
	v_mul_f32_e32 v30, v31, v24
	v_fmamk_f32 v24, v133, 0x3a000000, v9
	v_min_f32_e32 v24, 0x40e00000, v24
	v_mul_f32_e32 v32, 0x3fd9db23, v24
	v_mul_f32_e32 v32, 0xbfb8aa3b, v32
	v_fmamk_f32 v31, v101, 0x3a000000, v5
	v_exp_f32_e32 v32, v32
	v_med3_f32 v31, v31, s55, v199
	v_fma_f32 v31, v31, 4.0, 4.0
	v_mul_f32_e32 v31, v24, v31
	v_add_f32_e32 v24, 1.0, v32
	v_rcp_f32_e32 v32, v24
	v_mov_b32_e32 v24, v171
	v_cvt_pk_fp8_f32 v24, v23, v25
	v_ashrrev_i32_e32 v23, 31, v22
	v_lshlrev_b64 v[22:23], 11, v[22:23]
	v_mov_b32_e32 v25, v171
	v_lshl_add_u64 v[22:23], s[22:23], 0, v[22:23]
	v_cvt_pk_fp8_f32 v25, v28, v26
	v_lshl_add_u64 v[20:21], v[22:23], 0, v[20:21]
	v_fmamk_f32 v22, v94, 0x3a000000, v14
	v_min_f32_e32 v22, 0x40e00000, v22
	v_mul_f32_e32 v23, 0x3fd9db23, v22
	v_mul_f32_e32 v26, v32, v31
	v_mul_f32_e32 v23, 0xbfb8aa3b, v23
	v_cvt_pk_fp8_f32 v24, v27, v30 op_sel:[0,0,1]
	v_cvt_pk_fp8_f32 v25, v29, v26 op_sel:[0,0,1]
	v_exp_f32_e32 v23, v23
	global_store_dwordx2 v[20:21], v[24:25], off
	v_fmamk_f32 v20, v62, 0x3a000000, v10
	v_add_f32_e32 v21, 1.0, v23
	v_med3_f32 v20, v20, s55, v199
	v_rcp_f32_e32 v21, v21
	v_fma_f32 v20, v20, 4.0, 4.0
	v_mul_f32_e32 v20, v22, v20
	v_mul_f32_e32 v21, v21, v20
	v_fmamk_f32 v20, v90, 0x3a000000, v6
	v_min_f32_e32 v20, 0x40e00000, v20
	v_mul_f32_e32 v23, 0x3fd9db23, v20
	v_mul_f32_e32 v23, 0xbfb8aa3b, v23
	v_fmamk_f32 v22, v58, 0x3a000000, v2
	v_exp_f32_e32 v23, v23
	v_med3_f32 v22, v22, s55, v199
	v_fma_f32 v22, v22, 4.0, 4.0
	v_mul_f32_e32 v20, v20, v22
	v_add_f32_e32 v22, 1.0, v23
	v_fmamk_f32 v23, v95, 0x3a000000, v15
	v_min_f32_e32 v23, 0x40e00000, v23
	v_mul_f32_e32 v24, 0x3fd9db23, v23
	v_mul_f32_e32 v24, 0xbfb8aa3b, v24
	v_rcp_f32_e32 v22, v22
	v_exp_f32_e32 v24, v24
	v_mul_f32_e32 v22, v22, v20
	v_fmamk_f32 v20, v63, 0x3a000000, v11
	v_add_f32_e32 v24, 1.0, v24
	v_med3_f32 v20, v20, s55, v199
	v_rcp_f32_e32 v24, v24
	v_fma_f32 v20, v20, 4.0, 4.0
	v_mul_f32_e32 v20, v23, v20
	v_mul_f32_e32 v23, v24, v20
	v_fmamk_f32 v20, v91, 0x3a000000, v7
	v_min_f32_e32 v20, 0x40e00000, v20
	v_mul_f32_e32 v25, 0x3fd9db23, v20
	v_mul_f32_e32 v25, 0xbfb8aa3b, v25
	v_fmamk_f32 v24, v59, 0x3a000000, v3
	v_exp_f32_e32 v25, v25
	v_med3_f32 v24, v24, s55, v199
	v_fma_f32 v24, v24, 4.0, 4.0
	v_mul_f32_e32 v20, v20, v24
	v_add_f32_e32 v24, 1.0, v25
	v_fmamk_f32 v25, v96, 0x3a000000, v16
	v_min_f32_e32 v25, 0x40e00000, v25
	v_mul_f32_e32 v26, 0x3fd9db23, v25
	v_mul_f32_e32 v26, 0xbfb8aa3b, v26
	v_rcp_f32_e32 v24, v24
	v_exp_f32_e32 v26, v26
	v_mul_f32_e32 v24, v24, v20
	v_fmamk_f32 v20, v64, 0x3a000000, v12
	v_add_f32_e32 v26, 1.0, v26
	v_med3_f32 v20, v20, s55, v199
	v_rcp_f32_e32 v26, v26
	v_fma_f32 v20, v20, 4.0, 4.0
	v_mul_f32_e32 v20, v25, v20
	v_mul_f32_e32 v25, v26, v20
	v_fmamk_f32 v20, v92, 0x3a000000, v8
	v_min_f32_e32 v20, 0x40e00000, v20
	v_mul_f32_e32 v27, 0x3fd9db23, v20
; __device__ __forceinline__ unsigned pk4f8(float a, float b, float c, float d) { int r = 0; r = __builtin_amdgcn_cvt_pk_fp8_f32(a, b, r, false); r = __builtin_amdgcn_cvt_pk_fp8_f32(c, d, r, true); return (unsigned)r; }
; __device__ __forceinline__ float sigm(float x) { return __builtin_amdgcn_rcpf(1.f + __expf(-x)); }
;     __device__ __forceinline__ void operator()(const f32x4 (&acc)[2][2][4][2], const Unit& u, int wr, int wc, int fr, int fq) const {
;     ...
;             for (int m = 0; m < 4; ++m) { const size_t r = (size_t)(row0 + ai * HALF + m * 16);
;                 constexpr float DS = 1.f / (F8_SX * F8_SW);
;                 const f32x4 ga = acc[ai][0][m][0] * DS + bg0, gb = acc[ai][0][m][1] * DS + bg1, ua = acc[ai][1][m][0] * DS + bu0, ub = acc[ai][1][m][1] * DS + bu1;
;                 float o[8];
; #pragma unroll
;                 for (int j = 0; j < 4; ++j) { const float g = fminf(ga[j], 7.f), up = fminf(fmaxf(ua[j], -7.f), 7.f); o[j] = F8_SA * (up + 1.f) * g * sigm(1.702f * g);
;                                               const float g2 = fminf(gb[j], 7.f), up2 = fminf(fmaxf(ub[j], -7.f), 7.f); o[4 + j] = F8_SA * (up2 + 1.f) * g2 * sigm(1.702f * g2); }
;                 v2u w; w.x = pk4f8(o[0], o[1], o[2], o[3]); w.y = pk4f8(o[4], o[5], o[6], o[7]);
;                 *(v2u*)(ACT + r * FF + colg) = w; }
	v_mul_f32_e32 v27, 0xbfb8aa3b, v27
	v_fmamk_f32 v26, v60, 0x3a000000, v4
	v_exp_f32_e32 v27, v27
	v_med3_f32 v26, v26, s55, v199
	v_fma_f32 v26, v26, 4.0, 4.0
	v_mul_f32_e32 v20, v20, v26
	v_add_f32_e32 v26, 1.0, v27
	v_fmamk_f32 v27, v97, 0x3a000000, v17
	v_min_f32_e32 v27, 0x40e00000, v27
	v_mul_f32_e32 v28, 0x3fd9db23, v27
	v_mul_f32_e32 v28, 0xbfb8aa3b, v28
	v_rcp_f32_e32 v26, v26
	v_exp_f32_e32 v28, v28
	v_mul_f32_e32 v26, v26, v20
	v_fmamk_f32 v20, v65, 0x3a000000, v13
	v_add_f32_e32 v28, 1.0, v28
	v_med3_f32 v20, v20, s55, v199
	v_rcp_f32_e32 v28, v28
	v_fma_f32 v20, v20, 4.0, 4.0
	v_mul_f32_e32 v20, v27, v20
	v_mul_f32_e32 v27, v28, v20
	v_fmamk_f32 v20, v93, 0x3a000000, v9
	v_min_f32_e32 v28, 0x40e00000, v20
	v_mul_f32_e32 v29, 0x3fd9db23, v28
	v_mul_f32_e32 v29, 0xbfb8aa3b, v29
	v_exp_f32_e32 v29, v29
	v_fmamk_f32 v20, v61, 0x3a000000, v5
	v_med3_f32 v20, v20, s55, v199
	v_add_f32_e32 v20, 1.0, v20
	v_mul_f32_e32 v30, 4.0, v20
	v_add_f32_e32 v20, 1.0, v29
	v_rcp_f32_e32 v29, v20
	v_mov_b32_e32 v20, v171
	v_cvt_pk_fp8_f32 v20, v21, v23
	v_mov_b32_e32 v21, v171
	v_cvt_pk_fp8_f32 v21, v22, v24
	v_fmamk_f32 v24, v86, 0x3a000000, v14
	v_min_f32_e32 v24, 0x40e00000, v24
	v_mul_f32_e32 v22, v28, v30
	v_cvt_pk_fp8_f32 v20, v25, v27 op_sel:[0,0,1]
	v_mul_f32_e32 v25, 0x3fd9db23, v24
	v_mul_f32_e32 v22, v29, v22
	v_mul_f32_e32 v25, 0xbfb8aa3b, v25
	v_cvt_pk_fp8_f32 v21, v26, v22 op_sel:[0,0,1]
	v_exp_f32_e32 v25, v25
	v_add_co_u32_e32 v22, vcc, s56, v18
	s_nop 1
	v_addc_co_u32_e32 v23, vcc, 0, v19, vcc
	global_store_dwordx2 v[22:23], v[20:21], off
	v_fmamk_f32 v20, v54, 0x3a000000, v10
	v_add_f32_e32 v21, 1.0, v25
	v_med3_f32 v20, v20, s55, v199
	v_rcp_f32_e32 v21, v21
	v_fma_f32 v20, v20, 4.0, 4.0
	v_mul_f32_e32 v20, v24, v20
	v_mul_f32_e32 v21, v21, v20
	v_fmamk_f32 v20, v82, 0x3a000000, v6
	v_min_f32_e32 v20, 0x40e00000, v20
	v_mul_f32_e32 v23, 0x3fd9db23, v20
	v_mul_f32_e32 v23, 0xbfb8aa3b, v23
	v_fmamk_f32 v22, v50, 0x3a000000, v2
	v_exp_f32_e32 v23, v23
	v_med3_f32 v22, v22, s55, v199
	v_fma_f32 v22, v22, 4.0, 4.0
	v_mul_f32_e32 v20, v20, v22
	v_add_f32_e32 v22, 1.0, v23
	v_fmamk_f32 v23, v87, 0x3a000000, v15
	v_min_f32_e32 v23, 0x40e00000, v23
	v_mul_f32_e32 v24, 0x3fd9db23, v23
	v_mul_f32_e32 v24, 0xbfb8aa3b, v24
	v_rcp_f32_e32 v22, v22
	v_exp_f32_e32 v24, v24
	v_mul_f32_e32 v22, v22, v20
	v_fmamk_f32 v20, v55, 0x3a000000, v11
	v_add_f32_e32 v24, 1.0, v24
	v_med3_f32 v20, v20, s55, v199
	v_rcp_f32_e32 v24, v24
	v_fma_f32 v20, v20, 4.0, 4.0
	v_mul_f32_e32 v20, v23, v20
	v_mul_f32_e32 v23, v24, v20
	v_fmamk_f32 v20, v83, 0x3a000000, v7
	v_min_f32_e32 v20, 0x40e00000, v20
	v_mul_f32_e32 v25, 0x3fd9db23, v20
	v_mul_f32_e32 v25, 0xbfb8aa3b, v25
	v_fmamk_f32 v24, v51, 0x3a000000, v3
	v_exp_f32_e32 v25, v25
	v_med3_f32 v24, v24, s55, v199
	v_fma_f32 v24, v24, 4.0, 4.0
	v_mul_f32_e32 v20, v20, v24
	v_add_f32_e32 v24, 1.0, v25
	v_fmamk_f32 v25, v88, 0x3a000000, v16
	v_min_f32_e32 v25, 0x40e00000, v25
	v_mul_f32_e32 v26, 0x3fd9db23, v25
	v_mul_f32_e32 v26, 0xbfb8aa3b, v26
	v_rcp_f32_e32 v24, v24
	v_exp_f32_e32 v26, v26
	v_mul_f32_e32 v24, v24, v20
	v_fmamk_f32 v20, v56, 0x3a000000, v12
	v_add_f32_e32 v26, 1.0, v26
	v_med3_f32 v20, v20, s55, v199
	v_rcp_f32_e32 v26, v26
	v_fma_f32 v20, v20, 4.0, 4.0
	v_mul_f32_e32 v20, v25, v20
	v_mul_f32_e32 v25, v26, v20
	v_fmamk_f32 v20, v84, 0x3a000000, v8
	v_min_f32_e32 v20, 0x40e00000, v20
	v_mul_f32_e32 v27, 0x3fd9db23, v20
	v_mul_f32_e32 v27, 0xbfb8aa3b, v27
	v_fmamk_f32 v26, v52, 0x3a000000, v4
	v_exp_f32_e32 v27, v27
	v_med3_f32 v26, v26, s55, v199
	v_fma_f32 v26, v26, 4.0, 4.0
	v_mul_f32_e32 v20, v20, v26
	v_add_f32_e32 v26, 1.0, v27
	v_fmamk_f32 v27, v89, 0x3a000000, v17
	v_min_f32_e32 v27, 0x40e00000, v27
	v_mul_f32_e32 v28, 0x3fd9db23, v27
	v_mul_f32_e32 v28, 0xbfb8aa3b, v28
	v_rcp_f32_e32 v26, v26
	v_exp_f32_e32 v28, v28
	v_mul_f32_e32 v26, v26, v20
	v_fmamk_f32 v20, v57, 0x3a000000, v13
	v_add_f32_e32 v28, 1.0, v28
	v_med3_f32 v20, v20, s55, v199
	v_rcp_f32_e32 v28, v28
	v_fma_f32 v20, v20, 4.0, 4.0
	v_mul_f32_e32 v20, v27, v20
	v_mul_f32_e32 v27, v28, v20
	v_fmamk_f32 v20, v85, 0x3a000000, v9
	v_min_f32_e32 v28, 0x40e00000, v20
	v_mul_f32_e32 v29, 0x3fd9db23, v28
	v_mul_f32_e32 v29, 0xbfb8aa3b, v29
	v_exp_f32_e32 v29, v29
	v_fmamk_f32 v20, v53, 0x3a000000, v5
	v_med3_f32 v20, v20, s55, v199
	v_add_f32_e32 v20, 1.0, v20
	v_mul_f32_e32 v30, 4.0, v20
	v_add_f32_e32 v20, 1.0, v29
	v_rcp_f32_e32 v29, v20
	v_mov_b32_e32 v20, v171
	v_cvt_pk_fp8_f32 v20, v21, v23
	v_mov_b32_e32 v21, v171
	v_cvt_pk_fp8_f32 v21, v22, v24
	v_fmamk_f32 v24, v78, 0x3a000000, v14
	v_min_f32_e32 v24, 0x40e00000, v24
	v_mul_f32_e32 v22, v28, v30
	v_cvt_pk_fp8_f32 v20, v25, v27 op_sel:[0,0,1]
	v_mul_f32_e32 v25, 0x3fd9db23, v24
	v_mul_f32_e32 v22, v29, v22
	v_mul_f32_e32 v25, 0xbfb8aa3b, v25
	v_cvt_pk_fp8_f32 v21, v26, v22 op_sel:[0,0,1]
	v_exp_f32_e32 v25, v25
	v_add_co_u32_e32 v22, vcc, s57, v18
	v_fmamk_f32 v14, v70, 0x3a000000, v14
	s_nop 0
	v_addc_co_u32_e32 v23, vcc, 0, v19, vcc
	global_store_dwordx2 v[22:23], v[20:21], off
	v_fmamk_f32 v20, v46, 0x3a000000, v10
	v_add_f32_e32 v21, 1.0, v25
	v_med3_f32 v20, v20, s55, v199
	v_rcp_f32_e32 v21, v21
	v_fma_f32 v20, v20, 4.0, 4.0
	v_mul_f32_e32 v20, v24, v20
	v_mul_f32_e32 v21, v21, v20
	v_fmamk_f32 v20, v74, 0x3a000000, v6
	v_min_f32_e32 v20, 0x40e00000, v20
	v_mul_f32_e32 v23, 0x3fd9db23, v20
	v_mul_f32_e32 v23, 0xbfb8aa3b, v23
	v_fmamk_f32 v22, v42, 0x3a000000, v2
	v_exp_f32_e32 v23, v23
	v_med3_f32 v22, v22, s55, v199
	v_fma_f32 v22, v22, 4.0, 4.0
	v_mul_f32_e32 v20, v20, v22
	v_add_f32_e32 v22, 1.0, v23
	v_fmamk_f32 v23, v79, 0x3a000000, v15
	v_min_f32_e32 v23, 0x40e00000, v23
; #define PG8_BAR __builtin_amdgcn_s_barrier()
; __device__ __forceinline__ unsigned pk4f8(float a, float b, float c, float d) { int r = 0; r = __builtin_amdgcn_cvt_pk_fp8_f32(a, b, r, false); r = __builtin_amdgcn_cvt_pk_fp8_f32(c, d, r, true); return (unsigned)r; }
; __device__ __forceinline__ float sigm(float x) { return __builtin_amdgcn_rcpf(1.f + __expf(-x)); }
; template <class Epi, class Sched, bool ALIGN_EPI = false, bool SP2 = false, bool FP8 = false, bool I8 = false>
; __device__ __forceinline__ void gemm_phase(PG8_LAS unsigned char* lds, const Gemm g, const Sched& S, const Epi& E) {
;     ...
;         if (!has_next) break;
; #pragma unroll
;         for (int a = 0; a < 2; ++a)
; #pragma unroll
;             for (int b = 0; b < 2; ++b)
; #pragma unroll
;                 for (int m = 0; m < 4; ++m)
; #pragma unroll
;                     for (int n = 0; n < 2; ++n) acc[a][b][m][n] = (f32x4){0.f, 0.f, 0.f, 0.f};
;         cur = nxt; cA = nA; cB = nB; ++ui;
;         if constexpr (ALIGN_EPI) { if (wr == 1) PG8_BAR; }
;     __device__ __forceinline__ void operator()(const f32x4 (&acc)[2][2][4][2], const Unit& u, int wr, int wc, int fr, int fq) const {
;     ...
;             for (int m = 0; m < 4; ++m) { const size_t r = (size_t)(row0 + ai * HALF + m * 16);
;                 constexpr float DS = 1.f / (F8_SX * F8_SW);
;                 const f32x4 ga = acc[ai][0][m][0] * DS + bg0, gb = acc[ai][0][m][1] * DS + bg1, ua = acc[ai][1][m][0] * DS + bu0, ub = acc[ai][1][m][1] * DS + bu1;
;                 float o[8];
; #pragma unroll
;                 for (int j = 0; j < 4; ++j) { const float g = fminf(ga[j], 7.f), up = fminf(fmaxf(ua[j], -7.f), 7.f); o[j] = F8_SA * (up + 1.f) * g * sigm(1.702f * g);
;                                               const float g2 = fminf(gb[j], 7.f), up2 = fminf(fmaxf(ub[j], -7.f), 7.f); o[4 + j] = F8_SA * (up2 + 1.f) * g2 * sigm(1.702f * g2); }
;                 v2u w; w.x = pk4f8(o[0], o[1], o[2], o[3]); w.y = pk4f8(o[4], o[5], o[6], o[7]);
;                 *(v2u*)(ACT + r * FF + colg) = w; }
	v_mul_f32_e32 v24, 0x3fd9db23, v23
	v_mul_f32_e32 v24, 0xbfb8aa3b, v24
	v_rcp_f32_e32 v22, v22
	v_exp_f32_e32 v24, v24
	v_fmamk_f32 v10, v38, 0x3a000000, v10
	v_med3_f32 v10, v10, s55, v199
	v_mul_f32_e32 v22, v22, v20
	v_fmamk_f32 v20, v47, 0x3a000000, v11
	v_add_f32_e32 v24, 1.0, v24
	v_med3_f32 v20, v20, s55, v199
	v_rcp_f32_e32 v24, v24
	v_fma_f32 v20, v20, 4.0, 4.0
	v_mul_f32_e32 v20, v23, v20
	v_mul_f32_e32 v23, v24, v20
	v_fmamk_f32 v20, v75, 0x3a000000, v7
	v_min_f32_e32 v20, 0x40e00000, v20
	v_mul_f32_e32 v25, 0x3fd9db23, v20
	v_mul_f32_e32 v25, 0xbfb8aa3b, v25
	v_fmamk_f32 v24, v43, 0x3a000000, v3
	v_exp_f32_e32 v25, v25
	v_med3_f32 v24, v24, s55, v199
	v_fma_f32 v24, v24, 4.0, 4.0
	v_mul_f32_e32 v20, v20, v24
	v_add_f32_e32 v24, 1.0, v25
	v_fmamk_f32 v25, v80, 0x3a000000, v16
	v_min_f32_e32 v25, 0x40e00000, v25
	v_mul_f32_e32 v26, 0x3fd9db23, v25
	v_mul_f32_e32 v26, 0xbfb8aa3b, v26
	v_rcp_f32_e32 v24, v24
	v_exp_f32_e32 v26, v26
	v_add_f32_e32 v10, 1.0, v10
	v_fmamk_f32 v6, v66, 0x3a000000, v6
	v_mul_f32_e32 v24, v24, v20
	v_fmamk_f32 v20, v48, 0x3a000000, v12
	v_add_f32_e32 v26, 1.0, v26
	v_med3_f32 v20, v20, s55, v199
	v_rcp_f32_e32 v26, v26
	v_fma_f32 v20, v20, 4.0, 4.0
	v_mul_f32_e32 v20, v25, v20
	v_mul_f32_e32 v25, v26, v20
	v_fmamk_f32 v20, v76, 0x3a000000, v8
	v_min_f32_e32 v20, 0x40e00000, v20
	v_mul_f32_e32 v27, 0x3fd9db23, v20
	v_mul_f32_e32 v27, 0xbfb8aa3b, v27
	v_fmamk_f32 v26, v44, 0x3a000000, v4
	v_exp_f32_e32 v27, v27
	v_med3_f32 v26, v26, s55, v199
	v_fma_f32 v26, v26, 4.0, 4.0
	v_mul_f32_e32 v20, v20, v26
	v_add_f32_e32 v26, 1.0, v27
	v_fmamk_f32 v27, v81, 0x3a000000, v17
	v_min_f32_e32 v27, 0x40e00000, v27
	v_mul_f32_e32 v28, 0x3fd9db23, v27
	v_mul_f32_e32 v28, 0xbfb8aa3b, v28
	v_rcp_f32_e32 v26, v26
	v_exp_f32_e32 v28, v28
	v_min_f32_e32 v14, 0x40e00000, v14
	v_mul_f32_e32 v10, 4.0, v10
	v_mul_f32_e32 v26, v26, v20
	v_fmamk_f32 v20, v49, 0x3a000000, v13
	v_add_f32_e32 v28, 1.0, v28
	v_med3_f32 v20, v20, s55, v199
	v_rcp_f32_e32 v28, v28
	v_fma_f32 v20, v20, 4.0, 4.0
	v_mul_f32_e32 v20, v27, v20
	v_mul_f32_e32 v27, v28, v20
	v_fmamk_f32 v20, v77, 0x3a000000, v9
	v_min_f32_e32 v28, 0x40e00000, v20
	v_mul_f32_e32 v29, 0x3fd9db23, v28
	v_mul_f32_e32 v29, 0xbfb8aa3b, v29
	v_exp_f32_e32 v29, v29
	v_fmamk_f32 v20, v45, 0x3a000000, v5
	v_med3_f32 v20, v20, s55, v199
	v_add_f32_e32 v20, 1.0, v20
	v_mul_f32_e32 v30, 4.0, v20
	v_add_f32_e32 v20, 1.0, v29
	v_rcp_f32_e32 v29, v20
	v_mov_b32_e32 v20, v171
	v_cvt_pk_fp8_f32 v20, v21, v23
	v_mov_b32_e32 v21, v171
	v_min_f32_e32 v6, 0x40e00000, v6
	v_cvt_pk_fp8_f32 v21, v22, v24
	v_mul_f32_e32 v24, 0x3fd9db23, v14
	v_mul_f32_e32 v10, v14, v10
	v_mul_f32_e32 v14, 0x3fd9db23, v6
	v_mul_f32_e32 v14, 0xbfb8aa3b, v14
	v_fmamk_f32 v2, v34, 0x3a000000, v2
	v_exp_f32_e32 v14, v14
	v_med3_f32 v2, v2, s55, v199
	v_fma_f32 v2, v2, 4.0, 4.0
	v_mul_f32_e32 v2, v6, v2
	v_add_f32_e32 v6, 1.0, v14
	v_fmamk_f32 v14, v71, 0x3a000000, v15
	v_min_f32_e32 v14, 0x40e00000, v14
	v_mul_f32_e32 v15, 0x3fd9db23, v14
	v_mul_f32_e32 v15, 0xbfb8aa3b, v15
	v_rcp_f32_e32 v6, v6
	v_exp_f32_e32 v15, v15
	v_fmamk_f32 v3, v35, 0x3a000000, v3
	v_med3_f32 v3, v3, s55, v199
	v_mul_f32_e32 v6, v6, v2
	v_fmamk_f32 v2, v39, 0x3a000000, v11
	v_add_f32_e32 v11, 1.0, v15
	v_med3_f32 v2, v2, s55, v199
	v_rcp_f32_e32 v11, v11
	v_fma_f32 v2, v2, 4.0, 4.0
	v_mul_f32_e32 v2, v14, v2
	v_mul_f32_e32 v11, v11, v2
	v_fmamk_f32 v2, v67, 0x3a000000, v7
	v_min_f32_e32 v2, 0x40e00000, v2
	v_mul_f32_e32 v7, 0x3fd9db23, v2
	v_mul_f32_e32 v7, 0xbfb8aa3b, v7
	v_exp_f32_e32 v7, v7
	v_fma_f32 v3, v3, 4.0, 4.0
	v_mul_f32_e32 v2, v2, v3
	v_add_f32_e32 v3, 1.0, v7
	v_fmamk_f32 v7, v72, 0x3a000000, v16
	v_min_f32_e32 v7, 0x40e00000, v7
	v_mul_f32_e32 v14, 0x3fd9db23, v7
	v_mul_f32_e32 v14, 0xbfb8aa3b, v14
	v_rcp_f32_e32 v3, v3
	v_exp_f32_e32 v14, v14
	v_fmac_f32_e32 v17, 0x3a000000, v73
	v_fmac_f32_e32 v13, 0x3a000000, v41
	v_mul_f32_e32 v15, v3, v2
	v_fmamk_f32 v2, v40, 0x3a000000, v12
	v_add_f32_e32 v3, 1.0, v14
	v_med3_f32 v2, v2, s55, v199
	v_rcp_f32_e32 v3, v3
	v_fma_f32 v2, v2, 4.0, 4.0
	v_mul_f32_e32 v2, v7, v2
	v_mul_f32_e32 v7, v3, v2
	v_fmamk_f32 v2, v68, 0x3a000000, v8
	v_min_f32_e32 v2, 0x40e00000, v2
	v_fmamk_f32 v3, v36, 0x3a000000, v4
	v_mul_f32_e32 v4, 0x3fd9db23, v2
	v_mul_f32_e32 v4, 0xbfb8aa3b, v4
	v_exp_f32_e32 v4, v4
	v_med3_f32 v3, v3, s55, v199
	v_fma_f32 v3, v3, 4.0, 4.0
	v_mul_f32_e32 v2, v2, v3
	v_add_f32_e32 v3, 1.0, v4
	v_min_f32_e32 v4, 0x40e00000, v17
	v_mul_f32_e32 v8, 0x3fd9db23, v4
	v_mul_f32_e32 v8, 0xbfb8aa3b, v8
	v_rcp_f32_e32 v3, v3
	v_exp_f32_e32 v8, v8
	v_mul_f32_e32 v22, v28, v30
	v_mul_f32_e32 v22, v29, v22
	v_mul_f32_e32 v12, v3, v2
	v_add_f32_e32 v3, 1.0, v8
	v_med3_f32 v2, v13, s55, v199
	v_rcp_f32_e32 v3, v3
	v_mul_f32_e32 v24, 0xbfb8aa3b, v24
	v_cvt_pk_fp8_f32 v20, v25, v27 op_sel:[0,0,1]
	v_cvt_pk_fp8_f32 v21, v26, v22 op_sel:[0,0,1]
	v_exp_f32_e32 v24, v24
	v_fma_f32 v2, v2, 4.0, 4.0
	v_fmac_f32_e32 v9, 0x3a000000, v69
	v_mul_f32_e32 v2, v4, v2
	v_min_f32_e32 v8, 0x40e00000, v9
	v_add_co_u32_e32 v22, vcc, s58, v18
	v_mul_f32_e32 v4, v3, v2
	v_mul_f32_e32 v2, 0x3fd9db23, v8
	v_addc_co_u32_e32 v23, vcc, 0, v19, vcc
	v_mul_f32_e32 v2, 0xbfb8aa3b, v2
	global_store_dwordx2 v[22:23], v[20:21], off
	v_add_f32_e32 v20, 1.0, v24
	v_exp_f32_e32 v2, v2
	v_rcp_f32_e32 v20, v20
	v_fmac_f32_e32 v5, 0x3a000000, v37
	v_med3_f32 v3, v5, s55, v199
	v_add_f32_e32 v3, 1.0, v3
	v_add_f32_e32 v2, 1.0, v2
	v_mul_f32_e32 v10, v20, v10
	v_mul_f32_e32 v5, 4.0, v3
	v_rcp_f32_e32 v9, v2
	v_mov_b32_e32 v2, v171
	v_mov_b32_e32 v3, v171
	v_cvt_pk_fp8_f32 v2, v10, v11
	v_cvt_pk_fp8_f32 v3, v6, v15
	v_mul_f32_e32 v5, v8, v5
	v_mul_f32_e32 v5, v9, v5
	v_cvt_pk_fp8_f32 v2, v7, v4 op_sel:[0,0,1]
	v_cvt_pk_fp8_f32 v3, v12, v5 op_sel:[0,0,1]
	v_add_co_u32_e32 v4, vcc, 0x58000, v18
	s_nop 1
	v_addc_co_u32_e32 v5, vcc, 0, v19, vcc
	s_and_b64 vcc, exec, s[6:7]
	global_store_dwordx2 v[4:5], v[2:3], off
	s_cbranch_vccnz .LBB0_1925
	s_andn2_b64 vcc, exec, s[20:21]
	s_cbranch_vccnz .LBB0_1911
	s_barrier
	s_branch .LBB0_1911
